# v12 + grid barrier: all workgroups watch the cross-XCC arrival counter reach (gen+1)*nx instead of the generation word bumped afterwards
# speedup vs baseline: 1.0009x; 1.0009x over previous
.LBB0_2787:
	s_or_b64 exec, exec, s[6:7]
	v_cvt_f32_u32_e32 v5, v3
	s_waitcnt vmcnt(0)
	v_readfirstlane_b32 s4, v4
	v_sub_u32_e32 v4, 0, v3
	v_rcp_iflag_f32_e32 v5, v5
	v_add_u32_e32 v6, s4, v2
	v_mul_f32_e32 v5, 0x4f7ffffe, v5
	v_cvt_u32_f32_e32 v5, v5
	v_mul_lo_u32 v2, v4, v5
	v_mul_hi_u32 v2, v5, v2
	v_add_u32_e32 v2, v5, v2
	v_mul_hi_u32 v2, v6, v2
	v_mul_lo_u32 v4, v2, v3
	v_sub_u32_e32 v4, v6, v4
	v_add_u32_e32 v5, 1, v2
	v_cmp_ge_u32_e32 vcc, v4, v3
	s_nop 1
	v_cndmask_b32_e32 v2, v2, v5, vcc
	v_sub_u32_e32 v5, v4, v3
	v_cndmask_b32_e32 v4, v4, v5, vcc
	v_add_u32_e32 v5, 1, v2
	v_cmp_ge_u32_e32 vcc, v4, v3
	v_add_u32_e32 v4, 1, v6
	s_nop 0
	v_cndmask_b32_e32 v2, v2, v5, vcc
	v_mul_lo_u32 v5, v3, v2
	v_add_u32_e32 v3, v5, v3
	v_cmp_ne_u32_e32 vcc, v4, v3
	s_and_saveexec_b64 s[4:5], vcc
	s_xor_b64 s[4:5], exec, s[4:5]
	s_cbranch_execz .LBB0_2801
	s_waitcnt lgkmcnt(0)
	v_mad_u32_u24 v2, v2, v1, v1
	v_mov_b32_e32 v1, 0x3000
	global_load_dword v1, v1, s[18:19] offset:1024 sc1
	s_add_u32 s8, s18, 0x3400
	s_addc_u32 s9, s19, 0
	s_waitcnt vmcnt(0)
	v_cmp_lt_u32_e32 vcc, v1, v2
	s_and_saveexec_b64 s[6:7], vcc
	s_cbranch_execz .LBB0_2800
	s_mov_b32 s24, 1
	s_mov_b64 s[10:11], 0
	v_mov_b32_e32 v1, 0
	s_branch .LBB0_2791

.LBB0_2793:
	global_load_dword v3, v1, s[8:9] sc1
	s_add_i32 s24, s24, 1
	s_mov_b64 s[20:21], -1
	s_waitcnt vmcnt(0)
	v_cmp_ge_u32_e32 vcc, v3, v2
	s_orn2_b64 s[14:15], vcc, exec
	s_branch .LBB0_2790

.LBB0_2804:
	s_or_b64 exec, exec, s[6:7]
	v_cvt_f32_u32_e32 v4, v1
	s_waitcnt vmcnt(0)
	v_readfirstlane_b32 s4, v3
	s_add_u32 s6, s18, 0x3500
	s_addc_u32 s7, s19, 0
	v_rcp_iflag_f32_e32 v4, v4
	v_add_u32_e32 v2, s4, v2
	v_add_u32_e32 v5, 1, v2
	s_mov_b64 s[8:9], -1
	v_mul_f32_e32 v3, 0x4f7ffffe, v4
	v_cvt_u32_f32_e32 v3, v3
	v_sub_u32_e32 v4, 0, v1
	v_mul_lo_u32 v4, v4, v3
	v_mul_hi_u32 v4, v3, v4
	v_add_u32_e32 v3, v3, v4
	v_mul_hi_u32 v3, v2, v3
	v_mul_lo_u32 v4, v3, v1
	v_sub_u32_e32 v2, v2, v4
	v_add_u32_e32 v6, 1, v3
	v_cmp_ge_u32_e32 vcc, v2, v1
	v_sub_u32_e32 v4, v2, v1
	s_nop 0
	v_cndmask_b32_e32 v3, v3, v6, vcc
	v_cndmask_b32_e32 v2, v2, v4, vcc
	v_add_u32_e32 v4, 1, v3
	v_cmp_ge_u32_e32 vcc, v2, v1
	s_nop 1
	v_cndmask_b32_e32 v4, v3, v4, vcc
	v_mul_lo_u32 v2, v1, v4
	v_add_u32_e32 v1, v2, v1
	v_cmp_ne_u32_e32 vcc, v5, v1
	v_mov_b32_e32 v4, v1
	v_mov_b64_e32 v[2:3], s[6:7]
	s_and_saveexec_b64 s[4:5], vcc
	s_cbranch_execz .LBB0_2816
	v_mov_b32_e32 v1, 0
	global_load_dword v2, v1, s[6:7] offset:-256 sc1
	s_mov_b64 s[12:13], 0
	s_waitcnt vmcnt(0)
	v_cmp_lt_u32_e32 vcc, v2, v4
	s_and_saveexec_b64 s[10:11], vcc
	s_cbranch_execz .LBB0_2815
	s_add_u32 s8, s18, 0x200
	s_addc_u32 s9, s19, 0
	s_mov_b32 s26, 1
	s_branch .LBB0_2808

.LBB0_2810:
	global_load_dword v2, v1, s[6:7] offset:-256 sc1
	s_add_i32 s26, s26, 1
	s_mov_b64 s[20:21], -1
	s_waitcnt vmcnt(0)
	v_cmp_ge_u32_e32 vcc, v2, v4
	s_orn2_b64 s[24:25], vcc, exec
	s_branch .LBB0_2807

.LBB0_2883:
	s_or_b64 exec, exec, s[4:5]
	v_cvt_f32_u32_e32 v6, v4
	s_waitcnt vmcnt(0)
	v_readfirstlane_b32 s3, v5
	v_sub_u32_e32 v5, 0, v4
	v_rcp_iflag_f32_e32 v6, v6
	v_add_u32_e32 v7, s3, v1
	v_mul_f32_e32 v6, 0x4f7ffffe, v6
	v_cvt_u32_f32_e32 v6, v6
	v_mul_lo_u32 v1, v5, v6
	v_mul_hi_u32 v1, v6, v1
	v_add_u32_e32 v1, v6, v1
	v_mul_hi_u32 v1, v7, v1
	v_mul_lo_u32 v5, v1, v4
	v_sub_u32_e32 v5, v7, v5
	v_add_u32_e32 v6, 1, v1
	v_cmp_ge_u32_e32 vcc, v5, v4
	s_nop 1
	v_cndmask_b32_e32 v1, v1, v6, vcc
	v_sub_u32_e32 v6, v5, v4
	v_cndmask_b32_e32 v5, v5, v6, vcc
	v_add_u32_e32 v6, 1, v1
	v_cmp_ge_u32_e32 vcc, v5, v4
	v_add_u32_e32 v5, 1, v7
	s_nop 0
	v_cndmask_b32_e32 v1, v1, v6, vcc
	v_mul_lo_u32 v6, v4, v1
	v_add_u32_e32 v4, v6, v4
	v_cmp_ne_u32_e32 vcc, v5, v4
	s_and_saveexec_b64 s[4:5], vcc
	s_xor_b64 s[4:5], exec, s[4:5]
	s_cbranch_execz .LBB0_2897
	v_readlane_b32 s8, v252, 47
	v_readlane_b32 s9, v252, 48
	s_waitcnt lgkmcnt(0)
	v_mad_u32_u24 v1, v1, v2, v2
	s_nop 3
	global_load_dword v2, v3, s[8:9] offset:-256 sc1
	s_waitcnt vmcnt(0)
	v_cmp_lt_u32_e32 vcc, v2, v1
	s_and_saveexec_b64 s[20:21], vcc
	s_cbranch_execz .LBB0_2896
	s_mov_b32 s3, 1
	s_mov_b64 s[24:25], 0
	s_branch .LBB0_2887

.LBB0_2889:
	v_readlane_b32 s8, v252, 47
	v_readlane_b32 s9, v252, 48
	s_add_i32 s3, s3, 1
	s_mov_b64 s[40:41], -1
	s_nop 2
	global_load_dword v2, v3, s[8:9] offset:-256 sc1
	s_waitcnt vmcnt(0)
	v_cmp_ge_u32_e32 vcc, v2, v1
	s_orn2_b64 s[38:39], vcc, exec
	s_branch .LBB0_2886

.LBB0_2900:
	s_or_b64 exec, exec, s[20:21]
	s_waitcnt vmcnt(0)
	v_readfirstlane_b32 s3, v4
	v_sub_u32_e32 v5, 0, v2
	v_readlane_b32 s4, v252, 47
	v_add_u32_e32 v4, s3, v1
	v_cvt_f32_u32_e32 v1, v2
	v_readlane_b32 s5, v252, 48
	s_mov_b64 s[20:21], -1
	v_rcp_iflag_f32_e32 v1, v1
	s_nop 0
	v_mul_f32_e32 v1, 0x4f7ffffe, v1
	v_cvt_u32_f32_e32 v1, v1
	v_mul_lo_u32 v5, v5, v1
	v_mul_hi_u32 v5, v1, v5
	v_add_u32_e32 v1, v1, v5
	v_mul_hi_u32 v1, v4, v1
	v_mul_lo_u32 v5, v1, v2
	v_sub_u32_e32 v5, v4, v5
	v_cmp_ge_u32_e32 vcc, v5, v2
	v_add_u32_e32 v6, 1, v1
	v_add_u32_e32 v4, 1, v4
	v_cndmask_b32_e32 v1, v1, v6, vcc
	v_sub_u32_e32 v6, v5, v2
	v_cndmask_b32_e32 v5, v5, v6, vcc
	v_cmp_ge_u32_e32 vcc, v5, v2
	v_add_u32_e32 v5, 1, v1
	s_nop 0
	v_cndmask_b32_e32 v1, v1, v5, vcc
	v_mul_lo_u32 v5, v2, v1
	v_add_u32_e32 v2, v5, v2
	v_cmp_ne_u32_e32 vcc, v4, v2
	v_mov_b32_e32 v1, v2
	v_mov_b64_e32 v[4:5], s[4:5]
	s_and_saveexec_b64 s[4:5], vcc
	s_cbranch_execz .LBB0_2912
	v_readlane_b32 s8, v252, 47
	v_readlane_b32 s9, v252, 48
	s_mov_b64 s[24:25], 0
	s_nop 3
	global_load_dword v2, v3, s[8:9] offset:-256 sc1
	s_waitcnt vmcnt(0)
	v_cmp_lt_u32_e32 vcc, v2, v1
	s_and_saveexec_b64 s[20:21], vcc
	s_cbranch_execz .LBB0_2911
	s_mov_b32 s3, 1
	s_branch .LBB0_2904

.LBB0_7092:
	s_or_b64 exec, exec, s[4:5]
	v_cvt_f32_u32_e32 v6, v4
	s_waitcnt vmcnt(0)
	v_readfirstlane_b32 s2, v5
	v_sub_u32_e32 v5, 0, v4
	v_rcp_iflag_f32_e32 v6, v6
	v_add_u32_e32 v7, s2, v1
	v_mul_f32_e32 v6, 0x4f7ffffe, v6
	v_cvt_u32_f32_e32 v6, v6
	v_mul_lo_u32 v1, v5, v6
	v_mul_hi_u32 v1, v6, v1
	v_add_u32_e32 v1, v6, v1
	v_mul_hi_u32 v1, v7, v1
	v_mul_lo_u32 v5, v1, v4
	v_sub_u32_e32 v5, v7, v5
	v_add_u32_e32 v6, 1, v1
	v_cmp_ge_u32_e32 vcc, v5, v4
	s_nop 1
	v_cndmask_b32_e32 v1, v1, v6, vcc
	v_sub_u32_e32 v6, v5, v4
	v_cndmask_b32_e32 v5, v5, v6, vcc
	v_add_u32_e32 v6, 1, v1
	v_cmp_ge_u32_e32 vcc, v5, v4
	v_add_u32_e32 v5, 1, v7
	s_nop 0
	v_cndmask_b32_e32 v1, v1, v6, vcc
	v_mul_lo_u32 v6, v4, v1
	v_add_u32_e32 v4, v6, v4
	v_cmp_ne_u32_e32 vcc, v5, v4
	s_and_saveexec_b64 s[2:3], vcc
	s_xor_b64 s[4:5], exec, s[2:3]
	s_cbranch_execz .LBB0_7106
	v_readlane_b32 s2, v252, 47
	v_readlane_b32 s3, v252, 48
	s_waitcnt lgkmcnt(0)
	v_mad_u32_u24 v1, v1, v2, v2
	s_nop 3
	global_load_dword v2, v3, s[2:3] offset:-256 sc1
	s_waitcnt vmcnt(0)
	v_cmp_lt_u32_e32 vcc, v2, v1
	s_and_saveexec_b64 s[20:21], vcc
	s_cbranch_execz .LBB0_7105
	s_mov_b32 s2, 1
	s_mov_b64 s[24:25], 0
	s_branch .LBB0_7096

.LBB0_7098:
	v_readlane_b32 s8, v252, 47
	v_readlane_b32 s9, v252, 48
	s_add_i32 s2, s2, 1
	s_mov_b64 s[40:41], -1
	s_nop 2
	global_load_dword v2, v3, s[8:9] offset:-256 sc1
	s_waitcnt vmcnt(0)
	v_cmp_ge_u32_e32 vcc, v2, v1
	s_orn2_b64 s[38:39], vcc, exec
	s_branch .LBB0_7095

.LBB0_7109:
	s_or_b64 exec, exec, s[20:21]
	s_waitcnt vmcnt(0)
	v_readfirstlane_b32 s2, v4
	v_sub_u32_e32 v5, 0, v2
	s_mov_b64 s[20:21], -1
	v_add_u32_e32 v4, s2, v1
	v_cvt_f32_u32_e32 v1, v2
	v_readlane_b32 s2, v252, 47
	v_readlane_b32 s3, v252, 48
	v_rcp_iflag_f32_e32 v1, v1
	s_nop 0
	v_mul_f32_e32 v1, 0x4f7ffffe, v1
	v_cvt_u32_f32_e32 v1, v1
	v_mul_lo_u32 v5, v5, v1
	v_mul_hi_u32 v5, v1, v5
	v_add_u32_e32 v1, v1, v5
	v_mul_hi_u32 v1, v4, v1
	v_mul_lo_u32 v5, v1, v2
	v_sub_u32_e32 v5, v4, v5
	v_cmp_ge_u32_e32 vcc, v5, v2
	v_add_u32_e32 v6, 1, v1
	v_add_u32_e32 v4, 1, v4
	v_cndmask_b32_e32 v1, v1, v6, vcc
	v_sub_u32_e32 v6, v5, v2
	v_cndmask_b32_e32 v5, v5, v6, vcc
	v_cmp_ge_u32_e32 vcc, v5, v2
	v_add_u32_e32 v5, 1, v1
	s_nop 0
	v_cndmask_b32_e32 v1, v1, v5, vcc
	v_mul_lo_u32 v5, v2, v1
	v_add_u32_e32 v2, v5, v2
	v_cmp_ne_u32_e32 vcc, v4, v2
	v_mov_b32_e32 v1, v2
	v_mov_b64_e32 v[4:5], s[2:3]
	s_and_saveexec_b64 s[4:5], vcc
	s_cbranch_execz .LBB0_7121
	v_readlane_b32 s2, v252, 47
	v_readlane_b32 s3, v252, 48
	s_mov_b64 s[24:25], 0
	s_nop 3
	global_load_dword v2, v3, s[2:3] offset:-256 sc1
	s_waitcnt vmcnt(0)
	v_cmp_lt_u32_e32 vcc, v2, v1
	s_and_saveexec_b64 s[20:21], vcc
	s_cbranch_execz .LBB0_7120
	s_mov_b32 s2, 1
	s_branch .LBB0_7113

.LBB0_10853:
	s_or_b64 exec, exec, s[4:5]
	v_cvt_f32_u32_e32 v6, v4
	s_waitcnt vmcnt(0)
	v_readfirstlane_b32 s2, v5
	v_sub_u32_e32 v5, 0, v4
	v_rcp_iflag_f32_e32 v6, v6
	v_add_u32_e32 v7, s2, v1
	v_mul_f32_e32 v6, 0x4f7ffffe, v6
	v_cvt_u32_f32_e32 v6, v6
	v_mul_lo_u32 v1, v5, v6
	v_mul_hi_u32 v1, v6, v1
	v_add_u32_e32 v1, v6, v1
	v_mul_hi_u32 v1, v7, v1
	v_mul_lo_u32 v5, v1, v4
	v_sub_u32_e32 v5, v7, v5
	v_add_u32_e32 v6, 1, v1
	v_cmp_ge_u32_e32 vcc, v5, v4
	s_nop 1
	v_cndmask_b32_e32 v1, v1, v6, vcc
	v_sub_u32_e32 v6, v5, v4
	v_cndmask_b32_e32 v5, v5, v6, vcc
	v_add_u32_e32 v6, 1, v1
	v_cmp_ge_u32_e32 vcc, v5, v4
	v_add_u32_e32 v5, 1, v7
	s_nop 0
	v_cndmask_b32_e32 v1, v1, v6, vcc
	v_mul_lo_u32 v6, v4, v1
	v_add_u32_e32 v4, v6, v4
	v_cmp_ne_u32_e32 vcc, v5, v4
	s_and_saveexec_b64 s[2:3], vcc
	s_xor_b64 s[4:5], exec, s[2:3]
	s_cbranch_execz .LBB0_10867
	v_readlane_b32 s2, v252, 47
	v_readlane_b32 s3, v252, 48
	s_waitcnt lgkmcnt(0)
	v_mad_u32_u24 v1, v1, v2, v2
	s_nop 3
	global_load_dword v2, v3, s[2:3] offset:-256 sc1
	s_waitcnt vmcnt(0)
	v_cmp_lt_u32_e32 vcc, v2, v1
	s_and_saveexec_b64 s[8:9], vcc
	s_cbranch_execz .LBB0_10866
	s_mov_b32 s2, 1
	s_mov_b64 s[20:21], 0
	s_branch .LBB0_10857

.LBB0_10859:
	v_readlane_b32 s10, v252, 47
	v_readlane_b32 s11, v252, 48
	s_add_i32 s2, s2, 1
	s_mov_b64 s[38:39], -1
	s_nop 2
	global_load_dword v2, v3, s[10:11] offset:-256 sc1
	s_waitcnt vmcnt(0)
	v_cmp_ge_u32_e32 vcc, v2, v1
	s_orn2_b64 s[26:27], vcc, exec
	s_branch .LBB0_10856

.LBB0_10870:
	s_or_b64 exec, exec, s[8:9]
	s_waitcnt vmcnt(0)
	v_readfirstlane_b32 s2, v4
	v_sub_u32_e32 v5, 0, v2
	s_mov_b64 s[8:9], -1
	v_add_u32_e32 v4, s2, v1
	v_cvt_f32_u32_e32 v1, v2
	v_readlane_b32 s2, v252, 47
	v_readlane_b32 s3, v252, 48
	v_rcp_iflag_f32_e32 v1, v1
	s_nop 0
	v_mul_f32_e32 v1, 0x4f7ffffe, v1
	v_cvt_u32_f32_e32 v1, v1
	v_mul_lo_u32 v5, v5, v1
	v_mul_hi_u32 v5, v1, v5
	v_add_u32_e32 v1, v1, v5
	v_mul_hi_u32 v1, v4, v1
	v_mul_lo_u32 v5, v1, v2
	v_sub_u32_e32 v5, v4, v5
	v_cmp_ge_u32_e32 vcc, v5, v2
	v_add_u32_e32 v6, 1, v1
	v_add_u32_e32 v4, 1, v4
	v_cndmask_b32_e32 v1, v1, v6, vcc
	v_sub_u32_e32 v6, v5, v2
	v_cndmask_b32_e32 v5, v5, v6, vcc
	v_cmp_ge_u32_e32 vcc, v5, v2
	v_add_u32_e32 v5, 1, v1
	s_nop 0
	v_cndmask_b32_e32 v1, v1, v5, vcc
	v_mul_lo_u32 v5, v2, v1
	v_add_u32_e32 v2, v5, v2
	v_cmp_ne_u32_e32 vcc, v4, v2
	v_mov_b32_e32 v1, v2
	v_mov_b64_e32 v[4:5], s[2:3]
	s_and_saveexec_b64 s[4:5], vcc
	s_cbranch_execz .LBB0_10882
	v_readlane_b32 s2, v252, 47
	v_readlane_b32 s3, v252, 48
	s_mov_b64 s[20:21], 0
	s_nop 3
	global_load_dword v2, v3, s[2:3] offset:-256 sc1
	s_waitcnt vmcnt(0)
	v_cmp_lt_u32_e32 vcc, v2, v1
	s_and_saveexec_b64 s[8:9], vcc
	s_cbranch_execz .LBB0_10881
	s_mov_b32 s2, 1
	s_branch .LBB0_10874
